# ssd_local state tile: 64 two-byte stores per lane replaced by an LDS transpose through the wave's consumed xd tile and 8 dwordx4 stores of 1 KiB
# speedup vs baseline: 1.0035x; 1.0001x over previous
.LBB0_493:
	s_or_b64 exec, exec, s[36:37]
	v_mov_b32_e32 v48, v209
	v_mov_b32_e32 v32, v209
	v_mov_b32_e32 v16, v209
	v_mov_b32_e32 v0, v209
	v_add_u32_e32 v80, v193, v195
	v_add_u32_e32 v81, v194, v195
	v_add_u32_e32 v82, v194, v196
	v_add_u32_e32 v83, v193, v196
	s_waitcnt lgkmcnt(0)
	s_barrier
	ds_read_b64_tr_b16 v[2:3], v80 offset:20480
	ds_read_b64_tr_b16 v[4:5], v80 offset:20992
	ds_read_b64_tr_b16 v[10:11], v81 offset:4096
	ds_read_b64_tr_b16 v[12:13], v81 offset:4608
	ds_read_b64_tr_b16 v[64:65], v82 offset:4096
	ds_read_b64_tr_b16 v[66:67], v82 offset:4608
	ds_read_b64_tr_b16 v[68:69], v83 offset:20480
	ds_read_b64_tr_b16 v[70:71], v83 offset:20992
	v_mov_b32_e32 v49, v48
	v_mov_b32_e32 v50, v48
	v_mov_b32_e32 v51, v48
	v_mov_b32_e32 v52, v48
	v_mov_b32_e32 v53, v48
	v_mov_b32_e32 v54, v48
	v_mov_b32_e32 v55, v48
	v_mov_b32_e32 v56, v48
	v_mov_b32_e32 v57, v48
	v_mov_b32_e32 v58, v48
	v_mov_b32_e32 v59, v48
	v_mov_b32_e32 v60, v48
	v_mov_b32_e32 v61, v48
	v_mov_b32_e32 v62, v48
	v_mov_b32_e32 v63, v48
	v_mov_b32_e32 v33, v32
	v_mov_b32_e32 v34, v32
	v_mov_b32_e32 v35, v32
	v_mov_b32_e32 v36, v32
	v_mov_b32_e32 v37, v32
	v_mov_b32_e32 v38, v32
	v_mov_b32_e32 v39, v32
	v_mov_b32_e32 v40, v32
	v_mov_b32_e32 v41, v32
	v_mov_b32_e32 v42, v32
	v_mov_b32_e32 v43, v32
	v_mov_b32_e32 v44, v32
	v_mov_b32_e32 v45, v32
	v_mov_b32_e32 v46, v32
	v_mov_b32_e32 v47, v32
	v_mov_b32_e32 v17, v16
	v_mov_b32_e32 v18, v16
	v_mov_b32_e32 v19, v16
	v_mov_b32_e32 v20, v16
	v_mov_b32_e32 v21, v16
	v_mov_b32_e32 v22, v16
	v_mov_b32_e32 v23, v16
	v_mov_b32_e32 v24, v16
	v_mov_b32_e32 v25, v16
	v_mov_b32_e32 v26, v16
	v_mov_b32_e32 v27, v16
	v_mov_b32_e32 v28, v16
	v_mov_b32_e32 v29, v16
	v_mov_b32_e32 v30, v16
	v_mov_b32_e32 v31, v16
	s_waitcnt lgkmcnt(4)
	v_mfma_f32_32x32x16_bf16 v[48:63], v[2:5], v[10:13], v[48:63]
	v_mov_b32_e32 v1, v0
	v_mov_b32_e32 v6, v0
	v_mov_b32_e32 v7, v0
	v_mov_b32_e32 v8, v0
	v_mov_b32_e32 v9, v0
	v_mov_b32_e32 v14, v0
	v_mov_b32_e32 v15, v0
	s_waitcnt lgkmcnt(2)
	v_mfma_f32_32x32x16_bf16 v[32:47], v[2:5], v[64:67], v[32:47]
	v_mov_b32_e32 v2, v0
	v_mov_b32_e32 v3, v0
	v_mov_b32_e32 v4, v0
	v_mov_b32_e32 v5, v0
	s_lshl_b32 s36, s55, 3
	s_add_i32 s36, s36, s22
	s_ashr_i32 s37, s36, 31
	s_waitcnt lgkmcnt(0)
	v_mfma_f32_32x32x16_bf16 v[16:31], v[68:71], v[10:13], v[16:31]
	v_mov_b32_e32 v10, v0
	v_mov_b32_e32 v11, v0
	v_mov_b32_e32 v12, v0
	v_mov_b32_e32 v13, v0
	s_lshl_b64 s[38:39], s[36:37], 13
	s_add_u32 s38, s47, s38
	s_addc_u32 s39, s48, s39
	v_mfma_f32_32x32x16_bf16 v[0:15], v[68:71], v[64:67], v[0:15]
	ds_read_b64_tr_b16 v[64:65], v80 offset:22528
	ds_read_b64_tr_b16 v[66:67], v80 offset:23040
	ds_read_b64_tr_b16 v[68:69], v81 offset:6144
	ds_read_b64_tr_b16 v[70:71], v81 offset:6656
	ds_read_b64_tr_b16 v[72:73], v82 offset:6144
	ds_read_b64_tr_b16 v[74:75], v82 offset:6656
	ds_read_b64_tr_b16 v[76:77], v83 offset:22528
	ds_read_b64_tr_b16 v[78:79], v83 offset:23040
	s_waitcnt lgkmcnt(4)
	v_mfma_f32_32x32x16_bf16 v[48:63], v[64:67], v[68:71], v[48:63]
	s_waitcnt lgkmcnt(2)
	v_mfma_f32_32x32x16_bf16 v[32:47], v[64:67], v[72:75], v[32:47]
	s_waitcnt lgkmcnt(0)
	v_mfma_f32_32x32x16_bf16 v[16:31], v[76:79], v[68:71], v[16:31]
	ds_read_b64_tr_b16 v[64:65], v80 offset:24576
	ds_read_b64_tr_b16 v[66:67], v80 offset:25088
	ds_read_b64_tr_b16 v[68:69], v81 offset:8192
	ds_read_b64_tr_b16 v[70:71], v81 offset:8704
	v_mfma_f32_32x32x16_bf16 v[0:15], v[76:79], v[72:75], v[0:15]
	ds_read_b64_tr_b16 v[72:73], v82 offset:8192
	ds_read_b64_tr_b16 v[74:75], v82 offset:8704
	ds_read_b64_tr_b16 v[76:77], v83 offset:24576
	ds_read_b64_tr_b16 v[78:79], v83 offset:25088
	s_waitcnt lgkmcnt(4)
	v_mfma_f32_32x32x16_bf16 v[48:63], v[64:67], v[68:71], v[48:63]
	s_waitcnt lgkmcnt(2)
	v_mfma_f32_32x32x16_bf16 v[32:47], v[64:67], v[72:75], v[32:47]
	s_waitcnt lgkmcnt(0)
	v_mfma_f32_32x32x16_bf16 v[16:31], v[76:79], v[68:71], v[16:31]
	ds_read_b64_tr_b16 v[64:65], v80 offset:26624
	ds_read_b64_tr_b16 v[66:67], v80 offset:27136
	ds_read_b64_tr_b16 v[68:69], v81 offset:10240
	ds_read_b64_tr_b16 v[70:71], v81 offset:10752
	s_waitcnt lgkmcnt(0)
	v_mfma_f32_32x32x16_bf16 v[48:63], v[64:67], v[68:71], v[48:63]
	v_mfma_f32_32x32x16_bf16 v[0:15], v[76:79], v[72:75], v[0:15]
	ds_read_b64_tr_b16 v[72:73], v82 offset:10240
	ds_read_b64_tr_b16 v[74:75], v82 offset:10752
	ds_read_b64_tr_b16 v[76:77], v83 offset:26624
	ds_read_b64_tr_b16 v[78:79], v83 offset:27136
	s_waitcnt lgkmcnt(2)
	v_mfma_f32_32x32x16_bf16 v[32:47], v[64:67], v[72:75], v[32:47]
	s_waitcnt lgkmcnt(0)
	v_mfma_f32_32x32x16_bf16 v[16:31], v[76:79], v[68:71], v[16:31]
	v_mfma_f32_32x32x16_bf16 v[0:15], v[76:79], v[72:75], v[0:15]
	s_lshl_b32 s98, s22, 13
	s_addk_i32 s98, 0x5000
	v_lshrrev_b32_e32 v64, 5, v85
	v_and_b32_e32 v65, 31, v85
	v_lshrrev_b32_e32 v80, 3, v65
	v_and_b32_e32 v81, 7, v65
	v_lshlrev_b32_e32 v81, 1, v81
	v_lshl_add_u32 v81, v64, 9, v81
	v_add_u32_e32 v81, s98, v81
	v_lshlrev_b32_e32 v82, 2, v64
	v_add_u32_e32 v83, 0, v82
	v_add_u32_e32 v66, 0, v80
	v_xor_b32_e32 v66, v66, v83
	v_lshl_add_u32 v66, v66, 4, v81
	v_add_u32_e32 v83, 1, v82
	v_add_u32_e32 v67, 0, v80
	v_xor_b32_e32 v67, v67, v83
	v_lshl_add_u32 v67, v67, 4, v81
	v_add_u32_e32 v83, 2, v82
	v_add_u32_e32 v68, 0, v80
	v_xor_b32_e32 v68, v68, v83
	v_lshl_add_u32 v68, v68, 4, v81
	v_add_u32_e32 v83, 3, v82
	v_add_u32_e32 v69, 0, v80
	v_xor_b32_e32 v69, v69, v83
	v_lshl_add_u32 v69, v69, 4, v81
	v_add_u32_e32 v83, 0, v82
	v_add_u32_e32 v70, 4, v80
	v_xor_b32_e32 v70, v70, v83
	v_lshl_add_u32 v70, v70, 4, v81
	v_add_u32_e32 v83, 1, v82
	v_add_u32_e32 v71, 4, v80
	v_xor_b32_e32 v71, v71, v83
	v_lshl_add_u32 v71, v71, 4, v81
	v_add_u32_e32 v83, 2, v82
	v_add_u32_e32 v72, 4, v80
	v_xor_b32_e32 v72, v72, v83
	v_lshl_add_u32 v72, v72, 4, v81
	v_add_u32_e32 v83, 3, v82
	v_add_u32_e32 v73, 4, v80
	v_xor_b32_e32 v73, v73, v83
	v_lshl_add_u32 v73, v73, 4, v81
	v_bfe_u32 v76, v48, 16, 1
	v_add3_u32 v48, v48, v76, s63
	v_bfe_u32 v77, v49, 16, 1
	v_add3_u32 v49, v49, v77, s63
	v_bfe_u32 v78, v50, 16, 1
	v_add3_u32 v50, v50, v78, s63
	v_bfe_u32 v79, v51, 16, 1
	v_add3_u32 v51, v51, v79, s63
	v_bfe_u32 v76, v52, 16, 1
	v_add3_u32 v52, v52, v76, s63
	v_bfe_u32 v77, v53, 16, 1
	v_add3_u32 v53, v53, v77, s63
	v_bfe_u32 v78, v54, 16, 1
	v_add3_u32 v54, v54, v78, s63
	v_bfe_u32 v79, v55, 16, 1
	v_add3_u32 v55, v55, v79, s63
	v_bfe_u32 v76, v56, 16, 1
	v_add3_u32 v56, v56, v76, s63
	v_bfe_u32 v77, v57, 16, 1
	v_add3_u32 v57, v57, v77, s63
	v_bfe_u32 v78, v58, 16, 1
	v_add3_u32 v58, v58, v78, s63
	v_bfe_u32 v79, v59, 16, 1
	v_add3_u32 v59, v59, v79, s63
	v_bfe_u32 v76, v60, 16, 1
	v_add3_u32 v60, v60, v76, s63
	v_bfe_u32 v77, v61, 16, 1
	v_add3_u32 v61, v61, v77, s63
	v_bfe_u32 v78, v62, 16, 1
	v_add3_u32 v62, v62, v78, s63
	v_bfe_u32 v79, v63, 16, 1
	v_add3_u32 v63, v63, v79, s63
	ds_write_b16_d16_hi v66, v48 offset:0
	ds_write_b16_d16_hi v67, v49 offset:128
	ds_write_b16_d16_hi v68, v50 offset:256
	ds_write_b16_d16_hi v69, v51 offset:384
	ds_write_b16_d16_hi v66, v52 offset:1024
	ds_write_b16_d16_hi v67, v53 offset:1152
	ds_write_b16_d16_hi v68, v54 offset:1280
	ds_write_b16_d16_hi v69, v55 offset:1408
	ds_write_b16_d16_hi v66, v56 offset:2048
	ds_write_b16_d16_hi v67, v57 offset:2176
	ds_write_b16_d16_hi v68, v58 offset:2304
	ds_write_b16_d16_hi v69, v59 offset:2432
	ds_write_b16_d16_hi v66, v60 offset:3072
	ds_write_b16_d16_hi v67, v61 offset:3200
	ds_write_b16_d16_hi v68, v62 offset:3328
	ds_write_b16_d16_hi v69, v63 offset:3456
	v_bfe_u32 v76, v32, 16, 1
	v_add3_u32 v32, v32, v76, s63
	v_bfe_u32 v77, v33, 16, 1
	v_add3_u32 v33, v33, v77, s63
	v_bfe_u32 v78, v34, 16, 1
	v_add3_u32 v34, v34, v78, s63
	v_bfe_u32 v79, v35, 16, 1
	v_add3_u32 v35, v35, v79, s63
	v_bfe_u32 v76, v36, 16, 1
	v_add3_u32 v36, v36, v76, s63
	v_bfe_u32 v77, v37, 16, 1
	v_add3_u32 v37, v37, v77, s63
	v_bfe_u32 v78, v38, 16, 1
	v_add3_u32 v38, v38, v78, s63
	v_bfe_u32 v79, v39, 16, 1
	v_add3_u32 v39, v39, v79, s63
	v_bfe_u32 v76, v40, 16, 1
	v_add3_u32 v40, v40, v76, s63
	v_bfe_u32 v77, v41, 16, 1
	v_add3_u32 v41, v41, v77, s63
	v_bfe_u32 v78, v42, 16, 1
	v_add3_u32 v42, v42, v78, s63
	v_bfe_u32 v79, v43, 16, 1
	v_add3_u32 v43, v43, v79, s63
	v_bfe_u32 v76, v44, 16, 1
	v_add3_u32 v44, v44, v76, s63
	v_bfe_u32 v77, v45, 16, 1
	v_add3_u32 v45, v45, v77, s63
	v_bfe_u32 v78, v46, 16, 1
	v_add3_u32 v46, v46, v78, s63
	v_bfe_u32 v79, v47, 16, 1
	v_add3_u32 v47, v47, v79, s63
	ds_write_b16_d16_hi v70, v32 offset:0
	ds_write_b16_d16_hi v71, v33 offset:128
	ds_write_b16_d16_hi v72, v34 offset:256
	ds_write_b16_d16_hi v73, v35 offset:384
	ds_write_b16_d16_hi v70, v36 offset:1024
	ds_write_b16_d16_hi v71, v37 offset:1152
	ds_write_b16_d16_hi v72, v38 offset:1280
	ds_write_b16_d16_hi v73, v39 offset:1408
	ds_write_b16_d16_hi v70, v40 offset:2048
	ds_write_b16_d16_hi v71, v41 offset:2176
	ds_write_b16_d16_hi v72, v42 offset:2304
	ds_write_b16_d16_hi v73, v43 offset:2432
	ds_write_b16_d16_hi v70, v44 offset:3072
	ds_write_b16_d16_hi v71, v45 offset:3200
	ds_write_b16_d16_hi v72, v46 offset:3328
	ds_write_b16_d16_hi v73, v47 offset:3456
	v_bfe_u32 v76, v16, 16, 1
	v_add3_u32 v16, v16, v76, s63
	v_bfe_u32 v77, v17, 16, 1
	v_add3_u32 v17, v17, v77, s63
	v_bfe_u32 v78, v18, 16, 1
	v_add3_u32 v18, v18, v78, s63
	v_bfe_u32 v79, v19, 16, 1
	v_add3_u32 v19, v19, v79, s63
	v_bfe_u32 v76, v20, 16, 1
	v_add3_u32 v20, v20, v76, s63
	v_bfe_u32 v77, v21, 16, 1
	v_add3_u32 v21, v21, v77, s63
	v_bfe_u32 v78, v22, 16, 1
	v_add3_u32 v22, v22, v78, s63
	v_bfe_u32 v79, v23, 16, 1
	v_add3_u32 v23, v23, v79, s63
	v_bfe_u32 v76, v24, 16, 1
	v_add3_u32 v24, v24, v76, s63
	v_bfe_u32 v77, v25, 16, 1
	v_add3_u32 v25, v25, v77, s63
	v_bfe_u32 v78, v26, 16, 1
	v_add3_u32 v26, v26, v78, s63
	v_bfe_u32 v79, v27, 16, 1
	v_add3_u32 v27, v27, v79, s63
	v_bfe_u32 v76, v28, 16, 1
	v_add3_u32 v28, v28, v76, s63
	v_bfe_u32 v77, v29, 16, 1
	v_add3_u32 v29, v29, v77, s63
	v_bfe_u32 v78, v30, 16, 1
	v_add3_u32 v30, v30, v78, s63
	v_bfe_u32 v79, v31, 16, 1
	v_add3_u32 v31, v31, v79, s63
	ds_write_b16_d16_hi v66, v16 offset:4096
	ds_write_b16_d16_hi v67, v17 offset:4224
	ds_write_b16_d16_hi v68, v18 offset:4352
	ds_write_b16_d16_hi v69, v19 offset:4480
	ds_write_b16_d16_hi v66, v20 offset:5120
	ds_write_b16_d16_hi v67, v21 offset:5248
	ds_write_b16_d16_hi v68, v22 offset:5376
	ds_write_b16_d16_hi v69, v23 offset:5504
	ds_write_b16_d16_hi v66, v24 offset:6144
	ds_write_b16_d16_hi v67, v25 offset:6272
	ds_write_b16_d16_hi v68, v26 offset:6400
	ds_write_b16_d16_hi v69, v27 offset:6528
	ds_write_b16_d16_hi v66, v28 offset:7168
	ds_write_b16_d16_hi v67, v29 offset:7296
	ds_write_b16_d16_hi v68, v30 offset:7424
	ds_write_b16_d16_hi v69, v31 offset:7552
	v_bfe_u32 v76, v0, 16, 1
	v_add3_u32 v0, v0, v76, s63
	v_bfe_u32 v77, v1, 16, 1
	v_add3_u32 v1, v1, v77, s63
	v_bfe_u32 v78, v2, 16, 1
	v_add3_u32 v2, v2, v78, s63
	v_bfe_u32 v79, v3, 16, 1
	v_add3_u32 v3, v3, v79, s63
	v_bfe_u32 v76, v4, 16, 1
	v_add3_u32 v4, v4, v76, s63
	v_bfe_u32 v77, v5, 16, 1
	v_add3_u32 v5, v5, v77, s63
	v_bfe_u32 v78, v6, 16, 1
	v_add3_u32 v6, v6, v78, s63
	v_bfe_u32 v79, v7, 16, 1
	v_add3_u32 v7, v7, v79, s63
	v_bfe_u32 v76, v8, 16, 1
	v_add3_u32 v8, v8, v76, s63
	v_bfe_u32 v77, v9, 16, 1
	v_add3_u32 v9, v9, v77, s63
	v_bfe_u32 v78, v10, 16, 1
	v_add3_u32 v10, v10, v78, s63
	v_bfe_u32 v79, v11, 16, 1
	v_add3_u32 v11, v11, v79, s63
	v_bfe_u32 v76, v12, 16, 1
	v_add3_u32 v12, v12, v76, s63
	v_bfe_u32 v77, v13, 16, 1
	v_add3_u32 v13, v13, v77, s63
	v_bfe_u32 v78, v14, 16, 1
	v_add3_u32 v14, v14, v78, s63
	v_bfe_u32 v79, v15, 16, 1
	v_add3_u32 v15, v15, v79, s63
	ds_write_b16_d16_hi v70, v0 offset:4096
	ds_write_b16_d16_hi v71, v1 offset:4224
	ds_write_b16_d16_hi v72, v2 offset:4352
	ds_write_b16_d16_hi v73, v3 offset:4480
	ds_write_b16_d16_hi v70, v4 offset:5120
	ds_write_b16_d16_hi v71, v5 offset:5248
	ds_write_b16_d16_hi v72, v6 offset:5376
	ds_write_b16_d16_hi v73, v7 offset:5504
	ds_write_b16_d16_hi v70, v8 offset:6144
	ds_write_b16_d16_hi v71, v9 offset:6272
	ds_write_b16_d16_hi v72, v10 offset:6400
	ds_write_b16_d16_hi v73, v11 offset:6528
	ds_write_b16_d16_hi v70, v12 offset:7168
	ds_write_b16_d16_hi v71, v13 offset:7296
	ds_write_b16_d16_hi v72, v14 offset:7424
	ds_write_b16_d16_hi v73, v15 offset:7552
	v_lshrrev_b32_e32 v80, 3, v85
	v_and_b32_e32 v82, 7, v85
	v_xor_b32_e32 v82, v82, v80
	v_lshlrev_b32_e32 v82, 4, v82
	v_lshl_add_u32 v82, v80, 7, v82
	v_add_u32_e32 v82, s98, v82
	v_lshlrev_b32_e32 v74, 4, v85
	v_add_u32_e32 v75, 0x1000, v74
	ds_read_b128 v[0:3], v82
	ds_read_b128 v[4:7], v82 offset:1024
	ds_read_b128 v[8:11], v82 offset:2048
	ds_read_b128 v[12:15], v82 offset:3072
	ds_read_b128 v[16:19], v82 offset:4096
	ds_read_b128 v[20:23], v82 offset:5120
	ds_read_b128 v[24:27], v82 offset:6144
	ds_read_b128 v[28:31], v82 offset:7168
	s_waitcnt lgkmcnt(7)
	global_store_dwordx4 v74, v[0:3], s[38:39]
	s_waitcnt lgkmcnt(6)
	global_store_dwordx4 v74, v[4:7], s[38:39] offset:1024
	s_waitcnt lgkmcnt(5)
	global_store_dwordx4 v74, v[8:11], s[38:39] offset:2048
	s_waitcnt lgkmcnt(4)
	global_store_dwordx4 v74, v[12:15], s[38:39] offset:3072
	s_waitcnt lgkmcnt(3)
	global_store_dwordx4 v75, v[16:19], s[38:39]
	s_waitcnt lgkmcnt(2)
	global_store_dwordx4 v75, v[20:23], s[38:39] offset:1024
	s_waitcnt lgkmcnt(1)
	global_store_dwordx4 v75, v[24:27], s[38:39] offset:2048
	s_waitcnt lgkmcnt(0)
	global_store_dwordx4 v75, v[28:31], s[38:39] offset:3072
	s_and_saveexec_b64 s[38:39], s[20:21]
	s_cbranch_execz .LBB0_417
	v_mov_b32_e32 v0, s54
	ds_read_b32 v0, v0 offset:252
	s_lshl_b64 s[36:37], s[36:37], 2
	s_add_u32 s36, s49, s36
	s_addc_u32 s37, s50, s37
	s_waitcnt lgkmcnt(0)
	v_mul_f32_e32 v0, 0x3fb8aa3b, v0
	v_exp_f32_e32 v0, v0
	global_store_dword v209, v0, s[36:37]
	s_branch .LBB0_417
